# v14 + scan roles and chunkprep items assigned by sequence (XCD x = sequence x); XCD-local barriers for all seams from the z GEMM to the router phase (7 of 11 per layer)
# speedup vs baseline: 1.0514x; 1.0087x over previous
.LBB0_721:
	s_mov_b32 s4, 0
	s_nop 0
	v_writelane_b32 v255, s4, 49
	s_mov_b32 s4, 0
	s_nop 0
	v_writelane_b32 v255, s4, 42
	s_cmpk_lt_i32 s92, 0x400
	s_cselect_b64 s[4:5], -1, 0
	s_ashr_i32 s83, s92, 31
	v_writelane_b32 v253, s4, 11
	s_lshr_b32 s3, s83, 29
	s_mov_b32 s35, 0
	v_writelane_b32 v253, s5, 12
	s_add_i32 s4, s92, s3
	s_ashr_i32 s3, s4, 3
	s_and_b32 s4, s4, -8
	s_sub_i32 s4, s92, s4
	s_lshl_b32 s5, s4, 7
	s_cmpk_lt_i32 s92, 0x700
	s_cselect_b64 s[6:7], -1, 0
	v_writelane_b32 v253, s6, 13
	v_mov_b32_e32 v65, 0
	s_mov_b64 s[88:89], 0x80
	v_writelane_b32 v253, s7, 14
	s_mov_b32 s95, 0x437f0000
	v_readlane_b32 s8, v253, 2
	v_readlane_b32 s9, v253, 3
	s_add_u32 s6, s8, 0x4200
	s_addc_u32 s7, s9, 0
	v_readlane_b32 s10, v253, 4
	v_readlane_b32 s11, v253, 5
	v_writelane_b32 v253, s6, 15
	v_mov_b32_e32 v167, 1
	s_mov_b32 s28, 0x800000
	v_writelane_b32 v253, s7, 16
	s_add_u32 s6, s8, 0x4400
	s_addc_u32 s7, s9, 0
	v_writelane_b32 v253, s6, 17
	s_movk_i32 s31, 0x240
	s_mov_b32 s29, 0xf800000
	v_writelane_b32 v253, s7, 18
	s_add_u32 s6, s8, 0x4500
	s_addc_u32 s7, s9, 0
	v_writelane_b32 v253, s6, 19
	v_mov_b32_e32 v214, 0x260
	s_mov_b32 s94, 0xbf1b4598
	v_writelane_b32 v253, s7, 20
	s_add_u32 s6, s8, 0x4600
	s_addc_u32 s7, s9, 0
	v_writelane_b32 v253, s6, 21
	s_movk_i32 s30, 0x7fff
	v_mov_b32_e32 v215, 0xff61b1e6
	v_writelane_b32 v253, s7, 22
	s_add_u32 s6, s8, 0x4700
	s_addc_u32 s7, s9, 0
	v_writelane_b32 v253, s6, 23
	v_mov_b32_e32 v216, 8
	s_mov_b32 s36, 0x42800000
	v_writelane_b32 v253, s7, 24
	s_add_u32 s6, s8, 0x4800
	s_addc_u32 s7, s9, 0
	v_writelane_b32 v253, s6, 25
	v_mov_b32_e32 v217, 0x3a27c5ac
	v_mov_b32_e32 v218, 0x3727c5ac
	v_writelane_b32 v253, s7, 26
	s_add_u32 s6, s8, 0x4900
	s_addc_u32 s7, s9, 0
	v_writelane_b32 v253, s6, 27
	s_mov_b32 s90, 0xc0e00000
	v_mov_b64_e32 v[250:251], 0x6ff
	v_writelane_b32 v253, s7, 28
	s_add_u32 s6, s8, 0x4a00
	s_addc_u32 s7, s9, 0
	v_writelane_b32 v253, s6, 29
	v_mov_b32_e32 v219, 0x41b17218
	v_mov_b32_e32 v252, 0x7ff
	v_writelane_b32 v253, s7, 30
	s_add_u32 s6, s8, 0x4b00
	s_addc_u32 s7, s9, 0
	v_writelane_b32 v253, s6, 31
	v_mov_b32_e32 v224, 0xffffa800
	v_mov_b32_e32 v225, 0x43e00000
	v_writelane_b32 v253, s7, 32
	s_add_u32 s6, s8, 0x4c00
	s_addc_u32 s7, s9, 0
	v_writelane_b32 v253, s6, 33
	v_mov_b32_e32 v166, 0x358637bd
	v_mov_b64_e32 v[168:169], 0x100
	v_writelane_b32 v253, s7, 34
	s_add_u32 s6, s8, 0x4d00
	s_addc_u32 s7, s9, 0
	v_writelane_b32 v253, s6, 35
	v_mov_b64_e32 v[170:171], 0xff
	v_mov_b32_e32 v226, 0x40e00000
	v_writelane_b32 v253, s7, 36
	s_add_u32 s6, s8, 0x4e00
	s_addc_u32 s7, s9, 0
	v_writelane_b32 v253, s6, 37
	s_nop 1
	v_writelane_b32 v253, s7, 38
	s_add_u32 s6, s8, 0x4f00
	s_addc_u32 s7, s9, 0
	v_writelane_b32 v253, s6, 39
	s_nop 1
	v_writelane_b32 v253, s7, 40
	s_add_u32 s6, s8, 0x5000
	s_addc_u32 s7, s9, 0
	v_writelane_b32 v253, s6, 41
	s_nop 1
	v_writelane_b32 v253, s7, 42
	s_add_u32 s6, s8, 0x5100
	s_addc_u32 s7, s9, 0
	v_writelane_b32 v253, s6, 43
	s_nop 1
	v_writelane_b32 v253, s7, 44
	s_add_u32 s6, s8, 0x5200
	s_addc_u32 s7, s9, 0
	v_writelane_b32 v253, s6, 45
	s_nop 1
	v_writelane_b32 v253, s7, 46
	s_add_u32 s6, s8, 0x5300
	s_addc_u32 s7, s9, 0
	v_writelane_b32 v253, s6, 47
	s_cmp_eq_u32 s2, 15
	s_nop 0
	v_writelane_b32 v253, s7, 48
	s_cselect_b64 s[6:7], -1, 0
	v_writelane_b32 v253, s6, 49
	s_cmp_eq_u32 s2, 14
	s_nop 0
	v_writelane_b32 v253, s7, 50
	s_cselect_b64 s[6:7], -1, 0
	v_writelane_b32 v253, s6, 51
	s_cmp_eq_u32 s2, 13
	s_nop 0
	v_writelane_b32 v253, s7, 52
	s_cselect_b64 s[6:7], -1, 0
	v_writelane_b32 v253, s6, 53
	s_cmp_eq_u32 s2, 12
	s_nop 0
	v_writelane_b32 v253, s7, 54
	s_cselect_b64 s[6:7], -1, 0
	v_writelane_b32 v253, s6, 55
	s_cmp_eq_u32 s2, 11
	s_nop 0
	v_writelane_b32 v253, s7, 56
	s_cselect_b64 s[6:7], -1, 0
	v_writelane_b32 v253, s6, 57
	s_cmp_eq_u32 s2, 10
	s_nop 0
	v_writelane_b32 v253, s7, 58
	s_cselect_b64 s[6:7], -1, 0
	v_writelane_b32 v253, s6, 59
	s_cmp_eq_u32 s2, 9
	s_nop 0
	v_writelane_b32 v253, s7, 60
	s_cselect_b64 s[6:7], -1, 0
	v_writelane_b32 v253, s6, 61
	s_cmp_eq_u32 s2, 8
	s_nop 0
	v_writelane_b32 v253, s7, 62
	s_cselect_b64 s[6:7], -1, 0
	v_writelane_b32 v253, s6, 63
	s_cmp_eq_u32 s2, 7
	s_nop 0
	v_writelane_b32 v254, s7, 0
	s_cselect_b64 s[6:7], -1, 0
	v_writelane_b32 v254, s6, 1
	s_cmp_eq_u32 s2, 6
	s_nop 0
	v_writelane_b32 v254, s7, 2
	s_cselect_b64 s[6:7], -1, 0
	v_writelane_b32 v254, s6, 3
	s_cmp_eq_u32 s2, 5
	s_nop 0
	v_writelane_b32 v254, s7, 4
	s_cselect_b64 s[6:7], -1, 0
	v_writelane_b32 v254, s6, 5
	s_cmp_eq_u32 s2, 4
	s_nop 0
	v_writelane_b32 v254, s7, 6
	s_cselect_b64 s[6:7], -1, 0
	v_writelane_b32 v254, s6, 7
	s_cmp_eq_u32 s2, 3
	s_nop 0
	v_writelane_b32 v254, s7, 8
	s_cselect_b64 s[6:7], -1, 0
	v_writelane_b32 v254, s6, 9
	s_cmp_eq_u32 s2, 2
	s_nop 0
	v_writelane_b32 v254, s7, 10
	s_cselect_b64 s[6:7], -1, 0
	v_writelane_b32 v254, s6, 11
	s_cmp_eq_u32 s2, 1
	s_nop 0
	v_writelane_b32 v254, s7, 12
	s_cselect_b64 s[6:7], -1, 0
	v_writelane_b32 v254, s6, 13
	s_cmp_eq_u32 s2, 0
	s_nop 0
	v_writelane_b32 v254, s7, 14
	s_cselect_b64 s[6:7], -1, 0
	s_lshl_b32 s2, s2, 8
	s_add_u32 s0, s0, s2
	v_writelane_b32 v254, s6, 15
	s_addc_u32 s1, s1, 0
	s_mul_i32 s2, s4, 33
	v_writelane_b32 v254, s7, 16
	s_add_u32 s6, s0, 0x1400
	s_addc_u32 s7, s1, 0
	v_writelane_b32 v254, s6, 17
	s_add_u32 s0, s0, 0x2400
	s_addc_u32 s1, s1, 0
	v_writelane_b32 v254, s7, 18
	v_writelane_b32 v254, s0, 19
	v_cmp_eq_u32_e64 s[6:7], 0, v0
	s_nop 0
	v_writelane_b32 v254, s1, 20
	s_add_u32 s0, s8, 0x7400
	s_addc_u32 s1, s9, 0
	v_writelane_b32 v254, s0, 21
	s_nop 1
	v_writelane_b32 v254, s1, 22
	s_add_u32 s0, s8, 0x7500
	s_addc_u32 s1, s9, 0
	v_writelane_b32 v254, s0, 23
	s_cmpk_lt_i32 s92, 0x100
	s_nop 0
	v_writelane_b32 v254, s1, 24
	s_cselect_b64 s[0:1], -1, 0
	v_writelane_b32 v254, s0, 25
	s_nop 1
	v_writelane_b32 v254, s1, 26
	s_lshl_b32 s0, s4, 5
	s_cmp_lt_i32 s4, 0
	s_mul_i32 s1, s4, 0x81
	s_cselect_b32 s1, s1, s5
	s_movk_i32 s5, 0xe1
	s_cselect_b32 s5, s5, 0xe0
	s_cselect_b32 s2, s2, s0
	s_add_i32 s0, s1, s3
	s_ashr_i32 s1, s0, 31
	s_lshr_b32 s1, s1, 25
	v_writelane_b32 v254, s6, 27
	s_add_i32 s1, s0, s1
	s_add_i32 s84, 0, 0x14a00
	v_writelane_b32 v254, s7, 28
	s_ashr_i32 s6, s1, 7
	s_and_b32 s1, s1, 0xff80
	s_sub_i32 s1, s0, s1
	s_bfe_i32 s0, s1, 0x80000
	s_bfe_u32 s0, s0, 0x3000c
	s_add_i32 s7, s1, s0
	s_bfe_i32 s0, s7, 0x80000
	s_and_b32 s7, s7, 0xf8
	s_sub_i32 s1, s1, s7
	s_lshl_b32 s6, s6, 3
	s_sext_i32_i16 s8, s0
	s_sext_i32_i8 s1, s1
	s_add_i32 s10, s6, s1
	s_ashr_i32 s1, s8, 3
	v_writelane_b32 v254, s1, 29
	s_mov_b32 s6, s10
	s_ashr_i32 s11, s10, 31
	v_writelane_b32 v254, s6, 30
	s_lshr_b32 s0, s8, 3
	s_bfe_i64 s[0:1], s[0:1], 0x100000
	v_writelane_b32 v254, s7, 31
	s_lshl_b64 s[6:7], s[10:11], 18
	v_writelane_b32 v254, s6, 32
	s_lshl_b64 s[0:1], s[0:1], 18
	s_add_i32 s85, 0, 0x15200
	v_writelane_b32 v254, s7, 33
	v_writelane_b32 v254, s0, 34
	s_add_i32 s37, 0, 0x15a00
	s_add_i32 s96, 0, 0x16200
	v_writelane_b32 v254, s1, 35
	s_mul_i32 s0, s4, s5
	s_add_i32 s0, s0, s3
	s_mul_hi_i32 s1, s0, 0x92492493
	s_add_i32 s1, s1, s0
	s_lshr_b32 s4, s1, 31
	s_ashr_i32 s1, s1, 7
	s_add_i32 s1, s1, s4
	s_mul_i32 s4, s1, 0xe0
	s_sub_i32 s4, s0, s4
	s_bfe_u32 s0, s4, 0x3001c
	s_add_i32 s5, s4, s0
	s_sext_i32_i16 s6, s5
	s_and_b32 s5, s5, 0xfff8
	s_sub_i32 s4, s4, s5
	s_lshl_b32 s1, s1, 3
	s_sext_i32_i16 s4, s4
	s_add_i32 s8, s1, s4
	s_ashr_i32 s1, s6, 3
	v_writelane_b32 v254, s1, 36
	s_add_i32 s1, s2, s3
	s_ashr_i32 s2, s1, 31
	s_lshr_b32 s2, s2, 27
	s_add_i32 s2, s1, s2
	s_ashr_i32 s3, s2, 5
	s_and_b32 s2, s2, 0xffe0
	s_sub_i32 s1, s1, s2
	s_bfe_i32 s2, s1, 0x80000
	s_bfe_u32 s2, s2, 0x3000c
	s_add_i32 s4, s1, s2
	s_bfe_i32 s2, s4, 0x80000
	s_and_b32 s4, s4, 0xf8
	s_sub_i32 s1, s1, s4
	s_lshl_b32 s3, s3, 3
	s_sext_i32_i8 s1, s1
	s_lshr_b32 s0, s6, 3
	s_sext_i32_i16 s5, s2
	s_add_i32 s6, s3, s1
	s_lshr_b32 s2, s5, 3
	s_ashr_i32 s5, s5, 3
	s_ashr_i32 s7, s6, 31
	v_writelane_b32 v254, s5, 37
	s_lshl_b64 s[4:5], s[6:7], 18
	v_writelane_b32 v254, s4, 38
	s_bfe_i64 s[2:3], s[2:3], 0x100000
	s_ashr_i32 s9, s8, 31
	v_writelane_b32 v254, s5, 39
	s_lshl_b64 s[4:5], s[2:3], 18
	v_writelane_b32 v254, s4, 40
	s_bfe_i64 s[0:1], s[0:1], 0x100000
	s_lshl_b64 s[0:1], s[0:1], 19
	v_writelane_b32 v254, s5, 41
	s_mov_b32 s4, s8
	v_writelane_b32 v254, s4, 42
	s_add_i32 s97, 0, 0x16a00
	s_nop 0
	v_writelane_b32 v254, s5, 43
	s_lshl_b64 s[4:5], s[8:9], 19
	v_writelane_b32 v254, s4, 44
	s_nop 1
	v_writelane_b32 v254, s5, 45
	v_writelane_b32 v254, s0, 46
	s_add_i32 s4, 0, 0x20040
	s_nop 0
	v_writelane_b32 v254, s1, 47
	s_mov_b32 s0, s6
	v_writelane_b32 v254, s0, 48
	s_nop 1
	v_writelane_b32 v254, s1, 49
	s_lshl_b64 s[0:1], s[6:7], 17
	v_writelane_b32 v254, s0, 50
	s_mov_b32 s6, s35
	s_nop 0
	v_writelane_b32 v254, s1, 51
	s_lshl_b64 s[0:1], s[2:3], 17
	v_writelane_b32 v254, s0, 52
	s_add_i32 s2, 0, 0x10400
	s_mov_b32 s3, 0xc3e00000
	v_writelane_b32 v254, s1, 53
	s_mov_b64 s[0:1], 0
	v_writelane_b32 v254, s0, 54
	s_nop 1
	v_writelane_b32 v254, s1, 55
	s_add_i32 s0, 0, 0x11a00
	v_writelane_b32 v254, s0, 56
	s_add_i32 s0, 0, 0x17210
	v_writelane_b32 v254, s0, 57
	s_add_i32 s0, 0, 0x13000
	v_writelane_b32 v254, s0, 58
	s_add_i32 s0, 0, 0x20780
	v_writelane_b32 v254, s0, 59
	v_writelane_b32 v254, s2, 60
	s_add_i32 s2, 0, 0x20640
	v_writelane_b32 v254, s2, 61
	v_writelane_b32 v254, s4, 62
	s_add_i32 s4, 0, 0x20600
	v_writelane_b32 v254, s4, 63
	s_add_i32 s4, 0, 0x20740
	v_writelane_b32 v255, s4, 0
	v_writelane_b32 v255, s83, 1
	v_writelane_b32 v255, s92, 2
	s_movk_i32 s1, 0x5800
	s_mov_b32 s0, 0x3d808081
	s_add_i32 s2, 0, 0x206c0
	v_writelane_b32 v255, s86, 3
	s_branch .LBB0_725

.LBB0_951:
	s_andn2_b64 vcc, exec, s[4:5]
	s_cbranch_vccnz .LBB0_1357
	s_movk_i32 s32, 0x800
	s_cmpk_lg_u32 s91, 0x100
	s_cbranch_scc1 .Lcp_nomap
	s_lshr_b32 s32, s93, 5
	s_and_b32 s93, s93, 31
	s_lshl_b32 s32, s32, 8
	s_add_i32 s93, s93, s32
	s_addk_i32 s32, 0x100
	s_movk_i32 s91, 0x20
	s_mov_b32 s4, 1
	s_nop 0
	v_writelane_b32 v255, s4, 49
.Lcp_nomap:
	s_load_dwordx2 s[86:87], s[24:25], 0x170
	s_ashr_i32 s34, s82, 2
	s_waitcnt vmcnt(0)
	v_lshl_add_u32 v32, s82, 6, v29
	v_and_b32_e32 v30, 15, v29
	s_cmpk_lt_i32 s93, 0x800
	v_ashrrev_i32_e32 v1, 2, v29
	v_mov_b32_e32 v0, v65
	s_cselect_b64 s[10:11], -1, 0
	s_cmpk_gt_i32 s93, 0x7ff
	v_and_b32_e32 v36, 63, v29
	v_lshrrev_b32_e32 v8, 3, v32
	v_lshlrev_b32_e32 v64, 1, v30
	v_and_b32_e32 v6, -4, v1
	v_or_b32_e32 v4, 3, v1
	s_cbranch_scc1 .LBB0_954
	s_lshl_b32 s4, s93, 1
	s_add_i32 s7, s4, s34
	s_ashr_i32 s4, s7, 9
	s_and_b32 s6, s7, 0x1c0
	s_ashr_i32 s5, s4, 31
	s_lshl_b32 s7, s7, 5
	s_lshl_b64 s[4:5], s[4:5], 11
	s_and_b32 s7, s7, 0x7e0
	s_or_b32 s4, s4, s7
	v_and_or_b32 v2, v8, 24, s4
	v_mov_b32_e32 v3, s5
	v_lshlrev_b64 v[2:3], 9, v[2:3]
	v_or3_b32 v2, v2, v36, s6
	s_waitcnt lgkmcnt(0)
	v_lshl_add_u64 v[10:11], v[2:3], 2, s[86:87]
	s_mov_b32 s7, 0x64001000
	v_add_co_u32_e32 v22, vcc, s7, v10
	v_lshl_add_u64 v[2:3], v[2:3], 1, s[86:87]
	s_nop 0
	v_addc_co_u32_e32 v23, vcc, 0, v11, vcc
	s_mov_b32 s7, 0x5e001000
	v_add_co_u32_e32 v24, vcc, s7, v2
	s_mov_b64 s[8:9], 0x64000000
	s_nop 0
	v_addc_co_u32_e32 v25, vcc, 0, v3, vcc
	s_mov_b32 s7, 0x5f001000
	v_lshl_add_u64 v[12:13], v[10:11], 0, s[8:9]
	s_mov_b64 s[8:9], 0x5e000000
	v_add_co_u32_e32 v26, vcc, s7, v2
	v_lshl_add_u64 v[14:15], v[2:3], 0, s[8:9]
	s_mov_b64 s[8:9], 0x5f000000
	v_addc_co_u32_e32 v27, vcc, 0, v3, vcc
	s_mov_b32 s7, 0x61001000
	v_lshl_add_u64 v[16:17], v[2:3], 0, s[8:9]
	s_mov_b64 s[8:9], 0x61000000
	v_add_co_u32_e32 v34, vcc, s7, v2
	v_lshl_add_u64 v[18:19], v[2:3], 0, s[8:9]
	s_mov_b64 s[8:9], 0x62000000
	v_addc_co_u32_e32 v35, vcc, 0, v3, vcc
	s_mov_b32 s7, 0x62001000
	v_lshl_add_u64 v[20:21], v[2:3], 0, s[8:9]
	v_add_co_u32_e32 v2, vcc, s7, v2
	s_mov_b32 s7, 0x64002000
	s_nop 0
	v_addc_co_u32_e32 v3, vcc, 0, v3, vcc
	global_load_dword v33, v[22:23], off offset:-4096 nt
	global_load_ushort v37, v[24:25], off offset:-4096 nt
	global_load_ushort v38, v[26:27], off offset:-4096 nt
	global_load_ushort v40, v[34:35], off offset:-4096 nt
	global_load_ushort v42, v[2:3], off offset:-4096 nt
	global_load_dword v87, v[12:13], off offset:2048 nt
	global_load_ushort v88, v[14:15], off offset:1024 nt
	global_load_ushort v39, v[16:17], off offset:1024 nt
	global_load_ushort v41, v[18:19], off offset:1024 nt
	global_load_ushort v43, v[20:21], off offset:1024 nt
	global_load_dword v89, v[22:23], off nt
	global_load_ushort v90, v[14:15], off offset:2048 nt
	global_load_ushort v44, v[16:17], off offset:2048 nt
	global_load_ushort v46, v[18:19], off offset:2048 nt
	global_load_ushort v48, v[20:21], off offset:2048 nt
	global_load_dword v91, v[22:23], off offset:2048 nt
	global_load_ushort v92, v[14:15], off offset:3072 nt
	global_load_ushort v45, v[16:17], off offset:3072 nt
	global_load_ushort v47, v[18:19], off offset:3072 nt
	global_load_ushort v49, v[20:21], off offset:3072 nt
	v_add_co_u32_e32 v12, vcc, s7, v10
	s_mov_b32 s7, 0x64003000
	s_nop 0
	v_addc_co_u32_e32 v13, vcc, 0, v11, vcc
	v_add_co_u32_e32 v10, vcc, s7, v10
	s_lshl_b64 s[4:5], s[4:5], 10
	s_nop 0
	v_addc_co_u32_e32 v11, vcc, 0, v11, vcc
	global_load_dword v93, v[10:11], off offset:-4096 nt
	global_load_ushort v98, v[24:25], off nt
	global_load_ushort v50, v[26:27], off nt
	global_load_ushort v52, v[34:35], off nt
	global_load_ushort v54, v[2:3], off nt
	global_load_dword v99, v[12:13], off offset:2048 nt
	global_load_ushort v100, v[24:25], off offset:1024 nt
	global_load_ushort v51, v[26:27], off offset:1024 nt
	global_load_ushort v53, v[34:35], off offset:1024 nt
	global_load_ushort v55, v[2:3], off offset:1024 nt
	global_load_dword v101, v[10:11], off nt
	global_load_ushort v102, v[24:25], off offset:2048 nt
	global_load_ushort v56, v[26:27], off offset:2048 nt
	global_load_ushort v58, v[34:35], off offset:2048 nt
	global_load_ushort v60, v[2:3], off offset:2048 nt
	global_load_dword v103, v[10:11], off offset:2048 nt
	global_load_ushort v104, v[24:25], off offset:3072 nt
	global_load_ushort v57, v[26:27], off offset:3072 nt
	global_load_ushort v59, v[34:35], off offset:3072 nt
	global_load_ushort v61, v[2:3], off offset:3072 nt
	s_add_u32 s4, s86, s4
	s_addc_u32 s5, s87, s5
	s_lshl_b32 s6, s6, 1
	s_add_u32 s4, s4, s6
	s_addc_u32 s5, s5, 0
	s_lshl_b32 s6, s82, 5
	s_and_b32 s6, s6, 0x60
	s_add_u32 s4, s4, s6
	s_addc_u32 s5, s5, 0
	v_lshl_add_u64 v[2:3], s[4:5], 0, v[64:65]
	s_mov_b64 s[4:5], 0x60000000
	v_ashrrev_i32_e32 v7, 31, v6
	v_lshl_add_u64 v[2:3], v[2:3], 0, s[4:5]
	v_lshlrev_b64 v[10:11], 10, v[6:7]
	v_or_b32_e32 v12, 1, v6
	v_lshl_add_u64 v[10:11], v[2:3], 0, v[10:11]
	s_movk_i32 s4, 0x4000
	v_ashrrev_i32_e32 v13, 31, v12
	global_load_ushort v83, v[10:11], off
	v_add_co_u32_e32 v10, vcc, s4, v10
	v_lshlrev_b64 v[12:13], 10, v[12:13]
	s_nop 0
	v_addc_co_u32_e32 v11, vcc, 0, v11, vcc
	v_lshl_add_u64 v[12:13], v[2:3], 0, v[12:13]
	global_load_ushort v118, v[10:11], off
	global_load_ushort v120, v[12:13], off
	global_load_ushort v121, v[10:11], off offset:1024
	v_or_b32_e32 v12, 2, v6
	v_ashrrev_i32_e32 v13, 31, v12
	v_lshlrev_b64 v[12:13], 10, v[12:13]
	v_lshl_add_u64 v[12:13], v[2:3], 0, v[12:13]
	v_ashrrev_i32_e32 v5, 31, v4
	global_load_ushort v122, v[12:13], off
	global_load_ushort v123, v[10:11], off offset:2048
	v_lshlrev_b64 v[12:13], 10, v[4:5]
	v_lshl_add_u64 v[2:3], v[2:3], 0, v[12:13]
	global_load_ushort v124, v[2:3], off
	global_load_ushort v134, v[10:11], off offset:3072

.LBB0_956:
	s_add_i32 s20, s20, s91
	s_add_i32 s34, s34, s16
	s_add_i32 s18, s18, s19
	s_add_i32 s17, s17, s91
	s_cmp_lt_i32 s20, s32
	s_barrier
	s_cbranch_scc0 .LBB0_1173

.LBB0_959:
	s_or_b64 exec, exec, s[80:81]
	s_add_u32 s26, s24, s33
	s_addc_u32 s27, s25, 0
	v_lshl_add_u64 v[84:85], s[26:27], 0, v[34:35]
	v_add_co_u32_e32 v8, vcc, 0x4000, v84
	v_lshl_or_b32 v4, v120, 16, v83
	v_lshl_or_b32 v5, v124, 16, v122
	v_lshl_or_b32 v6, v121, 16, v118
	v_lshl_or_b32 v7, v134, 16, v123
	v_addc_co_u32_e32 v9, vcc, 0, v85, vcc
	s_cmp_ge_i32 s17, s32
	global_store_dwordx4 v[8:9], v[4:7], off offset:2048
	s_cbranch_scc1 .LBB0_961
	v_readlane_b32 s21, v255, 25
	s_add_i32 s21, s21, s34
	s_ashr_i32 s26, s21, 9
	s_ashr_i32 s27, s26, 31
	s_lshl_b64 s[80:81], s[26:27], 11
	s_and_b32 s26, s18, 0x7e0
	s_or_b32 s80, s80, s26
	v_mov_b32_e32 v5, s81
	v_or_b32_e32 v4, s80, v62
	v_lshlrev_b64 v[4:5], 9, v[4:5]
	s_and_b32 s21, s21, 0x1c0
	v_or_b32_e32 v4, v4, v36
	v_readlane_b32 s22, v255, 15
	v_or_b32_e32 v4, s21, v4
	v_readlane_b32 s23, v255, 16
	s_movk_i32 s26, 0x3000
	v_mov_b32_e32 v83, v65
	v_lshl_add_u64 v[6:7], v[4:5], 2, s[22:23]
	v_readlane_b32 s22, v255, 13
	v_lshlrev_b64 v[4:5], 1, v[4:5]
	v_readlane_b32 s23, v255, 14
	s_nop 1
	v_lshl_add_u64 v[8:9], s[22:23], 0, v[4:5]
	v_readlane_b32 s22, v255, 17
	v_readlane_b32 s23, v255, 18
	s_nop 1
	v_lshl_add_u64 v[10:11], s[22:23], 0, v[4:5]
	v_readlane_b32 s22, v255, 19
	v_readlane_b32 s23, v255, 20
	s_nop 1
	v_lshl_add_u64 v[12:13], s[22:23], 0, v[4:5]
	v_readlane_b32 s22, v255, 21
	v_readlane_b32 s23, v255, 22
	s_nop 1
	v_lshl_add_u64 v[4:5], s[22:23], 0, v[4:5]
	s_movk_i32 s23, 0x1000
	v_add_co_u32_e32 v14, vcc, s23, v6
	s_movk_i32 s22, 0x2000
	s_nop 0
	v_addc_co_u32_e32 v15, vcc, 0, v7, vcc
	v_add_co_u32_e32 v16, vcc, s22, v6
	global_load_dword v33, v[6:7], off nt
	global_load_ushort v37, v[8:9], off nt
	global_load_ushort v38, v[10:11], off nt
	global_load_ushort v40, v[12:13], off nt
	global_load_ushort v42, v[4:5], off nt
	global_load_dword v87, v[6:7], off offset:2048 nt
	global_load_ushort v88, v[8:9], off offset:1024 nt
	global_load_ushort v39, v[10:11], off offset:1024 nt
	global_load_ushort v41, v[12:13], off offset:1024 nt
	global_load_ushort v43, v[4:5], off offset:1024 nt
	v_addc_co_u32_e32 v17, vcc, 0, v7, vcc
	global_load_dword v89, v[16:17], off offset:-4096 nt
	global_load_ushort v90, v[8:9], off offset:2048 nt
	global_load_ushort v44, v[10:11], off offset:2048 nt
	global_load_ushort v46, v[12:13], off offset:2048 nt
	global_load_ushort v48, v[4:5], off offset:2048 nt
	global_load_dword v91, v[14:15], off offset:2048 nt
	global_load_ushort v92, v[8:9], off offset:3072 nt
	global_load_ushort v45, v[10:11], off offset:3072 nt
	global_load_ushort v47, v[12:13], off offset:3072 nt
	global_load_ushort v49, v[4:5], off offset:3072 nt
	global_load_dword v93, v[16:17], off nt
	v_add_co_u32_e32 v8, vcc, s23, v8
	v_readlane_b32 s22, v255, 23
	s_nop 0
	v_addc_co_u32_e32 v9, vcc, 0, v9, vcc
	v_add_co_u32_e32 v10, vcc, s23, v10
	global_load_ushort v98, v[8:9], off nt
	s_nop 0
	v_addc_co_u32_e32 v11, vcc, 0, v11, vcc
	v_add_co_u32_e32 v12, vcc, s23, v12
	global_load_ushort v50, v[10:11], off nt
	s_nop 0
	v_addc_co_u32_e32 v13, vcc, 0, v13, vcc
	v_add_co_u32_e32 v4, vcc, s23, v4
	global_load_ushort v52, v[12:13], off nt
	s_nop 0
	v_addc_co_u32_e32 v5, vcc, 0, v5, vcc
	v_add_co_u32_e32 v6, vcc, s26, v6
	s_lshl_b64 s[26:27], s[80:81], 10
	s_add_u32 s26, s22, s26
	v_readlane_b32 s22, v255, 24
	s_addc_u32 s27, s22, s27
	s_lshl_b32 s21, s21, 1
	s_add_u32 s21, s26, s21
	s_addc_u32 s27, s27, 0
	v_readlane_b32 s22, v255, 26
	s_add_u32 s26, s21, s22
	v_addc_co_u32_e32 v7, vcc, 0, v7, vcc
	s_addc_u32 s27, s27, 0
	global_load_ushort v54, v[4:5], off nt
	global_load_dword v99, v[16:17], off offset:2048 nt
	global_load_ushort v100, v[8:9], off offset:1024 nt
	global_load_ushort v51, v[10:11], off offset:1024 nt
	global_load_ushort v53, v[12:13], off offset:1024 nt
	global_load_ushort v55, v[4:5], off offset:1024 nt
	global_load_dword v101, v[6:7], off nt
	global_load_ushort v102, v[8:9], off offset:2048 nt
	global_load_ushort v56, v[10:11], off offset:2048 nt
	global_load_ushort v58, v[12:13], off offset:2048 nt
	global_load_ushort v60, v[4:5], off offset:2048 nt
	global_load_dword v103, v[6:7], off offset:2048 nt
	global_load_ushort v104, v[8:9], off offset:3072 nt
	global_load_ushort v57, v[10:11], off offset:3072 nt
	global_load_ushort v59, v[12:13], off offset:3072 nt
	global_load_ushort v61, v[4:5], off offset:3072 nt
	v_lshl_add_u64 v[4:5], s[26:27], 0, v[82:83]
	v_lshl_add_u64 v[6:7], v[4:5], 0, v[66:67]
	global_load_ushort v83, v[6:7], off
	v_lshl_add_u64 v[6:7], v[4:5], 0, v[68:69]
	global_load_ushort v118, v[6:7], off
	v_lshl_add_u64 v[6:7], v[4:5], 0, v[70:71]
	global_load_ushort v120, v[6:7], off
	v_lshl_add_u64 v[6:7], v[4:5], 0, v[72:73]
	global_load_ushort v121, v[6:7], off
	v_lshl_add_u64 v[6:7], v[4:5], 0, v[74:75]
	global_load_ushort v122, v[6:7], off
	v_lshl_add_u64 v[6:7], v[4:5], 0, v[76:77]
	global_load_ushort v123, v[6:7], off
	v_lshl_add_u64 v[6:7], v[4:5], 0, v[78:79]
	v_lshl_add_u64 v[4:5], v[4:5], 0, v[80:81]
	global_load_ushort v124, v[6:7], off
	global_load_ushort v134, v[4:5], off

.LBB0_1191:
	s_add_i32 s21, s21, s91
	s_add_i32 s18, s18, s19
	s_add_u32 s10, s10, s27
	s_addc_u32 s11, s11, s26
	s_add_i32 s20, s20, s91
	s_waitcnt vmcnt(5)
	v_mov_b64_e32 v[14:15], v[10:11]
	s_cmp_ge_i32 s21, s32
	v_mov_b64_e32 v[12:13], v[8:9]
	s_barrier
	s_cbranch_scc1 .LBB0_1241
.LBB0_1192:
	s_waitcnt vmcnt(4)
	v_lshlrev_b32_e32 v48, 16, v4
	v_mul_f32_e32 v48, 0xbfb8aa3b, v48
	v_exp_f32_e32 v48, v48
	s_cmp_lt_i32 s20, s32
	s_cselect_b32 s12, s20, -1
	s_and_b32 s13, s18, 0x180
	v_lshl_add_u32 v16, s13, 2, v58
	ds_read_b128 v[20:23], v16 offset:56320
	ds_read_b128 v[16:19], v16 offset:56336
	v_add_f32_e32 v48, 1.0, v48
	v_rcp_f32_e32 v71, v48
	s_mov_b32 s13, 0x3f317217
	s_waitcnt lgkmcnt(1)
	v_sub_f32_e32 v72, 1.0, v20
	s_mov_b32 s14, 0x7f800000
	v_fma_f32 v20, v72, v71, v20
	v_max_f32_e32 v20, 0x2081cea, v20
	v_cmp_gt_f32_e32 vcc, s28, v20
	v_and_b32_e32 v49, 0xffff0000, v4
	v_sub_f32_e32 v78, 1.0, v21
	v_cndmask_b32_e64 v48, 0, 32, vcc
	v_ldexp_f32 v20, v20, v48
	v_log_f32_e32 v20, v20
	v_lshlrev_b32_e32 v50, 16, v5
	v_sub_f32_e32 v77, 1.0, v22
	v_and_b32_e32 v51, 0xffff0000, v5
	v_mul_f32_e32 v48, 0x3f317217, v20
	v_fma_f32 v48, v20, s13, -v48
	v_fmac_f32_e32 v48, 0x3377d1cf, v20
	v_fmac_f32_e32 v48, 0x3f317217, v20
	v_cmp_lt_f32_e64 s[56:57], |v20|, s14
	v_sub_f32_e32 v75, 1.0, v23
	v_lshlrev_b32_e32 v53, 16, v6
	v_cndmask_b32_e64 v20, v20, v48, s[56:57]
	v_cndmask_b32_e32 v48, 0, v219, vcc
	v_sub_f32_e32 v20, v20, v48
	v_mul_f32_e32 v48, 0xbfb8aa3b, v49
	v_exp_f32_e32 v48, v48
	s_waitcnt lgkmcnt(0)
	v_sub_f32_e32 v49, 1.0, v16
	v_and_b32_e32 v55, 0xffff0000, v6
	v_lshlrev_b32_e32 v52, 16, v7
	v_add_f32_e32 v48, 1.0, v48
	v_rcp_f32_e32 v73, v48
	v_mul_f32_e32 v52, 0xbfb8aa3b, v52
	v_exp_f32_e32 v52, v52
	v_and_b32_e32 v54, 0xffff0000, v7
	v_fma_f32 v21, v78, v73, v21
	v_max_f32_e32 v21, 0x2081cea, v21
	v_cmp_gt_f32_e32 vcc, s28, v21
	v_add_f32_e32 v52, 1.0, v52
	v_rcp_f32_e32 v52, v52
	v_cndmask_b32_e64 v48, 0, 32, vcc
	v_ldexp_f32 v21, v21, v48
	v_log_f32_e32 v21, v21
	v_mul_f32_e32 v54, 0xbfb8aa3b, v54
	v_exp_f32_e32 v54, v54
	s_cmp_lt_i32 s12, 0
	v_mul_f32_e32 v48, 0x3f317217, v21
	v_fma_f32 v48, v21, s13, -v48
	v_fmac_f32_e32 v48, 0x3377d1cf, v21
	v_fmac_f32_e32 v48, 0x3f317217, v21
	v_cmp_lt_f32_e64 s[56:57], |v21|, s14
	v_add_f32_e32 v54, 1.0, v54
	v_rcp_f32_e32 v54, v54
	v_cndmask_b32_e64 v21, v21, v48, s[56:57]
	v_cndmask_b32_e32 v48, 0, v219, vcc
	v_sub_f32_e32 v21, v21, v48
	v_mul_f32_e32 v48, 0xbfb8aa3b, v50
	v_exp_f32_e32 v48, v48
	s_nop 0
	v_add_f32_e32 v48, 1.0, v48
	v_rcp_f32_e32 v76, v48
	s_nop 0
	v_fma_f32 v22, v77, v76, v22
	v_max_f32_e32 v22, 0x2081cea, v22
	v_cmp_gt_f32_e32 vcc, s28, v22
	s_nop 1
	v_cndmask_b32_e64 v48, 0, 32, vcc
	v_ldexp_f32 v22, v22, v48
	v_log_f32_e32 v22, v22
	s_nop 0
	v_mul_f32_e32 v48, 0x3f317217, v22
	v_fma_f32 v48, v22, s13, -v48
	v_fmac_f32_e32 v48, 0x3377d1cf, v22
	v_fmac_f32_e32 v48, 0x3f317217, v22
	v_cmp_lt_f32_e64 s[56:57], |v22|, s14
	s_nop 1
	v_cndmask_b32_e64 v22, v22, v48, s[56:57]
	v_cndmask_b32_e32 v48, 0, v219, vcc
	v_sub_f32_e32 v22, v22, v48
	v_mul_f32_e32 v48, 0xbfb8aa3b, v51
	v_exp_f32_e32 v48, v48
	v_sub_f32_e32 v51, 1.0, v17
	v_add_f32_e32 v48, 1.0, v48
	v_rcp_f32_e32 v74, v48
	s_nop 0
	v_fmac_f32_e32 v23, v75, v74
	v_max_f32_e32 v23, 0x2081cea, v23
	v_cmp_gt_f32_e32 vcc, s28, v23
	s_nop 1
	v_cndmask_b32_e64 v48, 0, 32, vcc
	v_ldexp_f32 v23, v23, v48
	v_log_f32_e32 v23, v23
	s_nop 0
	v_mul_f32_e32 v48, 0x3f317217, v23
	v_fma_f32 v48, v23, s13, -v48
	v_fmac_f32_e32 v48, 0x3377d1cf, v23
	v_fmac_f32_e32 v48, 0x3f317217, v23
	v_cmp_lt_f32_e64 s[56:57], |v23|, s14
	s_nop 1
	v_cndmask_b32_e64 v23, v23, v48, s[56:57]
	v_cndmask_b32_e32 v48, 0, v219, vcc
	v_sub_f32_e32 v23, v23, v48
	v_mul_f32_e32 v48, 0xbfb8aa3b, v53
	v_exp_f32_e32 v48, v48
	s_nop 0
	v_add_f32_e32 v48, 1.0, v48
	v_rcp_f32_e32 v48, v48
	s_nop 0
	v_fma_f32 v16, v48, v49, v16
	v_max_f32_e32 v16, 0x2081cea, v16
	v_cmp_gt_f32_e32 vcc, s28, v16
	s_nop 1
	v_cndmask_b32_e64 v50, 0, 32, vcc
	v_ldexp_f32 v16, v16, v50
	v_log_f32_e32 v16, v16
	s_nop 0
	v_mul_f32_e32 v50, 0x3f317217, v16
	v_fma_f32 v50, v16, s13, -v50
	v_fmac_f32_e32 v50, 0x3377d1cf, v16
	v_fmac_f32_e32 v50, 0x3f317217, v16
	v_cmp_lt_f32_e64 s[56:57], |v16|, s14
	s_nop 1
	v_cndmask_b32_e64 v16, v16, v50, s[56:57]
	v_cndmask_b32_e32 v50, 0, v219, vcc
	v_sub_f32_e32 v16, v16, v50
	v_mul_f32_e32 v50, 0xbfb8aa3b, v55
	v_exp_f32_e32 v50, v50
	s_nop 0
	v_add_f32_e32 v50, 1.0, v50
	v_rcp_f32_e32 v50, v50
	s_nop 0
	v_fma_f32 v17, v50, v51, v17
	v_max_f32_e32 v17, 0x2081cea, v17
	v_cmp_gt_f32_e32 vcc, s28, v17
	s_nop 1
	v_cndmask_b32_e64 v53, 0, 32, vcc
	v_ldexp_f32 v17, v17, v53
	v_log_f32_e32 v17, v17
	s_nop 0
	v_mul_f32_e32 v53, 0x3f317217, v17
	v_fma_f32 v53, v17, s13, -v53
	v_fmac_f32_e32 v53, 0x3377d1cf, v17
	v_fmac_f32_e32 v53, 0x3f317217, v17
	v_cmp_lt_f32_e64 s[56:57], |v17|, s14
	s_nop 1
	v_cndmask_b32_e64 v17, v17, v53, s[56:57]
	v_cndmask_b32_e32 v53, 0, v219, vcc
	v_sub_f32_e32 v17, v17, v53
	v_sub_f32_e32 v53, 1.0, v18
	v_fma_f32 v18, v52, v53, v18
	v_max_f32_e32 v18, 0x2081cea, v18
	v_cmp_gt_f32_e32 vcc, s28, v18
	s_nop 1
	v_cndmask_b32_e64 v55, 0, 32, vcc
	v_ldexp_f32 v18, v18, v55
	v_log_f32_e32 v18, v18
	s_nop 0
	v_mul_f32_e32 v55, 0x3f317217, v18
	v_fma_f32 v55, v18, s13, -v55
	v_fmac_f32_e32 v55, 0x3377d1cf, v18
	v_fmac_f32_e32 v55, 0x3f317217, v18
	v_cmp_lt_f32_e64 s[56:57], |v18|, s14
	s_nop 1
	v_cndmask_b32_e64 v18, v18, v55, s[56:57]
	v_cndmask_b32_e32 v55, 0, v219, vcc
	v_sub_f32_e32 v18, v18, v55
	v_sub_f32_e32 v55, 1.0, v19
	v_fmac_f32_e32 v19, v54, v55
	v_max_f32_e32 v19, 0x2081cea, v19
	v_cmp_gt_f32_e32 vcc, s28, v19
	s_nop 1
	v_cndmask_b32_e64 v79, 0, 32, vcc
	v_ldexp_f32 v19, v19, v79
	v_log_f32_e32 v19, v19
	s_nop 0
	v_mul_f32_e32 v79, 0x3f317217, v19
	v_fma_f32 v79, v19, s13, -v79
	v_fmac_f32_e32 v79, 0x3377d1cf, v19
	v_fmac_f32_e32 v79, 0x3f317217, v19
	v_cmp_lt_f32_e64 s[56:57], |v19|, s14
	s_nop 1
	v_cndmask_b32_e64 v19, v19, v79, s[56:57]
	v_cndmask_b32_e32 v79, 0, v219, vcc
	v_sub_f32_e32 v19, v19, v79
	ds_write_b128 v59, v[20:23] offset:37888
	ds_write_b128 v59, v[16:19] offset:37904
	s_waitcnt vmcnt(3)
	ds_write_b16 v60, v0 offset:27648
	ds_write_b16_d16_hi v60, v0 offset:27728
	ds_write_b16 v60, v1 offset:27808
	ds_write_b16_d16_hi v60, v1 offset:27888
	ds_write_b16 v60, v2 offset:27968
	ds_write_b16_d16_hi v60, v2 offset:28048
	ds_write_b16 v60, v3 offset:28128
	ds_write_b16_d16_hi v60, v3 offset:28208
	s_cbranch_scc1 .LBB0_1194
	s_lshr_b32 s34, s12, 8
	s_lshl_b32 s13, s12, 5
	s_lshl_b64 s[14:15], s[34:35], 11
	s_and_b32 s13, s13, 0x7e0
	s_or_b32 s14, s14, s13
	v_lshl_add_u64 v[0:1], s[14:15], 0, v[36:37]
	v_mov_b64_e32 v[2:3], s[86:87]
	v_mad_u64_u32 v[2:3], s[14:15], v0, s1, v[2:3]
	s_lshl_b32 s12, s12, 2
	v_mad_i32_i24 v3, v1, s1, v3
	s_and_b32 s34, s12, 0x300
	v_lshl_add_u64 v[0:1], v[2:3], 0, s[34:35]
	v_lshl_add_u64 v[0:1], v[0:1], 0, v[64:65]
	s_mov_b64 s[12:13], 0x48000e00
	v_lshl_add_u64 v[2:3], v[0:1], 0, s[12:13]
	v_add_co_u32_e32 v0, vcc, 0x48000000, v0
	s_nop 1
	v_addc_co_u32_e32 v1, vcc, 0, v1, vcc
	global_load_dwordx4 v[8:11], v[0:1], off offset:3584
	global_load_dwordx4 v[4:7], v[2:3], off offset:1024
	s_nop 0
	global_load_dwordx4 v[0:3], v[2:3], off offset:2048

.LBB0_1268:
	s_add_i32 s60, s60, s91
	s_cmp_ge_i32 s60, s32
	s_cselect_b64 s[18:19], -1, 0
	s_cmp_lt_i32 s60, s32
	s_cselect_b32 s20, s60, -1
	s_cmp_lt_i32 s20, 0
	s_cbranch_scc1 .LBB0_1285
	s_bfe_u32 s61, s20, 0x20006
	s_lshr_b32 s34, s20, 8
	s_lshl_b32 s20, s20, 5
	s_and_b32 s63, s20, 0x7e0
	s_add_i32 s64, s63, -3
	s_lshl_b64 s[20:21], s[34:35], 11
	s_lshl_b32 s62, s61, 7
	s_and_saveexec_b64 s[22:23], s[38:39]
	s_cbranch_execz .LBB0_1276
	v_mov_b32_e32 v64, v65
	v_add_u32_e32 v12, s64, v74
	v_mov_b32_e32 v66, v65
	v_mov_b32_e32 v67, v65
	v_mov_b64_e32 v[0:1], v[64:65]
	v_cmp_lt_i32_e32 vcc, -1, v12
	v_mov_b64_e32 v[2:3], v[66:67]
	s_and_saveexec_b64 s[24:25], vcc
	s_cbranch_execz .LBB0_1272
	v_mov_b32_e32 v13, v65
	v_lshl_add_u64 v[0:1], s[20:21], 0, v[12:13]
	v_mov_b64_e32 v[2:3], s[12:13]
	v_mad_u64_u32 v[2:3], s[66:67], v0, s1, v[2:3]
	v_mad_u32_u24 v3, v1, s1, v3
	v_lshlrev_b32_e32 v64, 1, v46
	v_lshl_add_u64 v[0:1], v[2:3], 0, v[64:65]
	s_lshl_b32 s34, s62, 1
	v_lshl_add_u64 v[0:1], v[0:1], 0, s[34:35]
	v_lshlrev_b32_e32 v64, 1, v40
	v_lshl_add_u64 v[0:1], v[0:1], 0, v[64:65]
	v_add_co_u32_e32 v0, vcc, 0x1000, v0
	s_nop 1
	v_addc_co_u32_e32 v1, vcc, 0, v1, vcc
	global_load_dwordx4 v[0:3], v[0:1], off offset:3584

.LBB0_1306:
	v_readlane_b32 s4, v255, 49
	s_nop 3
	s_cmp_eq_u32 s4, 1
	s_cbranch_scc0 .Lcp_norest
	s_mov_b32 s4, 0
	s_nop 0
	v_writelane_b32 v255, s4, 49
	v_readlane_b32 s4, v255, 2
	s_nop 3
	s_and_b32 s5, s4, 7
	s_lshl_b32 s5, s5, 5
	s_lshr_b32 s4, s4, 3
	s_add_i32 s93, s5, s4
	s_movk_i32 s91, 0x100

.LBB0_1359:
	s_andn2_b64 vcc, exec, s[4:5]
	s_cbranch_vccnz .LBB0_1641
	s_load_dwordx2 s[48:49], s[46:47], 0x170
	v_lshl_add_u32 v228, s82, 6, v227
	s_mov_b32 s18, s92
	s_cmpk_lg_u32 s91, 0x100
	s_cbranch_scc1 .Lscan_nomap
	s_and_b32 s8, s92, 7
	s_lshr_b32 s9, s92, 3
	s_cmp_gt_u32 s9, 3
	s_cbranch_scc1 .Lscan_r1
	s_lshl_b32 s18, s8, 2
	s_add_i32 s18, s18, s9
	s_branch .Lscan_nomap
.Lscan_r1:
	s_cmp_gt_u32 s9, 11
	s_cbranch_scc1 .Lscan_r2
	s_lshl_b32 s10, s8, 3
	s_add_i32 s10, s10, s9
	s_sub_i32 s10, s10, 4
	s_lshr_b32 s11, s10, 4
	s_lshl_b32 s11, s11, 4
	s_and_b32 s12, s10, 1
	s_lshl_b32 s12, s12, 3
	s_bfe_u32 s13, s10, 0x30001
	s_add_i32 s18, s11, s12
	s_add_i32 s18, s18, s13
	s_add_i32 s18, s18, 32
	s_branch .Lscan_nomap
.Lscan_r2:
	s_cmp_gt_u32 s9, 15
	s_cbranch_scc1 .Lscan_r3
	s_lshl_b32 s18, s8, 2
	s_add_i32 s18, s18, s9
	s_add_i32 s18, s18, 84
	s_branch .Lscan_nomap
.Lscan_r3:
	s_cmp_gt_u32 s9, 23
	s_cbranch_scc1 .Lscan_nomap
	s_lshl_b32 s18, s8, 3
	s_add_i32 s18, s18, s9
	s_add_i32 s18, s18, 112
.Lscan_nomap:
	s_cmpk_lt_i32 s91, 0xa0
	s_cbranch_scc1 .LBB0_1526
	s_cmp_gt_i32 s18, 31
	s_cbranch_scc0 .LBB0_1369
	s_cmpk_gt_u32 s18, 0x5f
	s_cbranch_scc0 .LBB0_1370
	s_cmpk_gt_u32 s18, 0x7f
	s_cbranch_scc0 .LBB0_1371
	s_mov_b64 s[4:5], 0
	s_cmpk_lt_u32 s18, 0xc0
	s_mov_b64 s[6:7], 0
	s_cbranch_scc0 .LBB0_1372
	s_add_i32 s9, s18, 0xffffff80
	v_ashrrev_i32_e32 v229, 4, v228
	s_lshl_b32 s7, s9, 8
	v_lshlrev_b32_e32 v158, 6, v229
	s_lshl_b32 s6, s9, 6
	s_and_b32 s34, s7, 0x3800
	v_ashrrev_i32_e32 v159, 31, v158
	s_and_b32 s6, s6, 0x1c0
	v_and_b32_e32 v161, 15, v227
	v_lshl_add_u64 v[172:173], s[34:35], 0, v[158:159]
	v_lshl_or_b32 v160, v161, 2, s6
	s_waitcnt vmcnt(0)
	v_lshlrev_b64 v[0:1], 11, v[172:173]
	s_waitcnt lgkmcnt(0)
	v_lshl_add_u64 v[0:1], s[48:49], 0, v[0:1]
	v_lshlrev_b32_e32 v32, 2, v160
	v_mov_b32_e32 v33, v65
	v_lshl_add_u64 v[16:17], v[0:1], 0, v[32:33]
	s_mov_b64 s[6:7], 0x6e200000
	v_lshl_add_u64 v[4:5], v[16:17], 0, s[6:7]
	v_lshlrev_b64 v[0:1], 10, v[172:173]
	s_mov_b32 s6, 0x6e201000
	v_lshl_add_u64 v[0:1], s[48:49], 0, v[0:1]
	v_lshlrev_b32_e32 v64, 1, v160
	v_add_co_u32_e32 v12, vcc, s6, v16
	v_lshl_add_u64 v[34:35], v[0:1], 0, v[64:65]
	s_nop 0
	v_addc_co_u32_e32 v13, vcc, 0, v17, vcc
	s_mov_b32 s6, 0x70201000
	v_add_co_u32_e32 v36, vcc, s6, v34
	s_mov_b32 s6, 0x6e202000
	s_nop 0
	v_addc_co_u32_e32 v37, vcc, 0, v35, vcc
	v_add_co_u32_e32 v20, vcc, s6, v16
	s_mov_b32 s6, 0x6e203000
	s_nop 0
	v_addc_co_u32_e32 v21, vcc, 0, v17, vcc
	v_add_co_u32_e32 v28, vcc, s6, v16
	s_mov_b64 s[6:7], 0x70200000
	global_load_dwordx4 v[0:3], v[12:13], off offset:-4096
	s_nop 0
	global_load_dwordx4 v[4:7], v[4:5], off offset:2048
	s_nop 0
	global_load_dwordx4 v[8:11], v[12:13], off
	s_nop 0
	global_load_dwordx4 v[12:15], v[12:13], off offset:2048
	v_addc_co_u32_e32 v29, vcc, 0, v17, vcc
	v_lshl_add_u64 v[34:35], v[34:35], 0, s[6:7]
	global_load_dwordx4 v[16:19], v[28:29], off offset:-4096
	s_nop 0
	global_load_dwordx4 v[20:23], v[20:21], off offset:2048
	s_nop 0
	global_load_dwordx4 v[24:27], v[28:29], off
	s_nop 0
	global_load_dwordx4 v[28:31], v[28:29], off offset:2048
	s_nop 0
	global_load_dwordx2 v[138:139], v[36:37], off offset:-4096
	global_load_dwordx2 v[140:141], v[34:35], off offset:1024
	global_load_dwordx2 v[142:143], v[34:35], off offset:2048
	global_load_dwordx2 v[144:145], v[34:35], off offset:3072
	global_load_dwordx2 v[148:149], v[36:37], off
	global_load_dwordx2 v[152:153], v[36:37], off offset:1024
	global_load_dwordx2 v[154:155], v[36:37], off offset:2048
	global_load_dwordx2 v[156:157], v[36:37], off offset:3072
	s_lshl_b32 s6, s9, 19
	s_lshl_b32 s7, s9, 18
	s_and_b32 s34, s6, 0x1c00000
	v_lshlrev_b64 v[34:35], 11, v[158:159]
	v_lshlrev_b64 v[36:37], 10, v[158:159]
	v_lshl_add_u64 v[146:147], s[34:35], 0, v[34:35]
	s_and_b32 s34, s7, 0xe00000
	v_lshl_add_u64 v[150:151], s[34:35], 0, v[36:37]
	v_mov_b32_e32 v48, 0
	v_mov_b32_e32 v52, 1.0
	v_or_b32_e32 v146, v146, v32
	v_or_b32_e32 v150, v150, v64
	s_mov_b32 s8, 0
	s_bfe_u32 s12, s9, 0x30003
	v_mov_b32_e32 v53, v52
	v_mov_b32_e32 v54, v52
	v_mov_b32_e32 v55, v52
	v_mov_b32_e32 v49, v48
	v_mov_b32_e32 v50, v48
	v_mov_b32_e32 v51, v48
	v_mov_b64_e32 v[174:175], v[146:147]
	v_mov_b64_e32 v[176:177], v[150:151]
	s_waitcnt vmcnt(14)
	v_mov_b64_e32 v[112:113], v[6:7]
	v_mov_b64_e32 v[120:121], v[2:3]
	s_waitcnt vmcnt(13)
	v_mov_b64_e32 v[100:101], v[10:11]
	s_waitcnt vmcnt(12)
	v_mov_b64_e32 v[96:97], v[14:15]
	s_waitcnt vmcnt(11)
	v_mov_b64_e32 v[88:89], v[18:19]
	s_waitcnt vmcnt(10)
	v_mov_b64_e32 v[84:85], v[22:23]
	s_waitcnt vmcnt(9)
	v_mov_b64_e32 v[80:81], v[26:27]
	s_waitcnt vmcnt(8)
	v_mov_b64_e32 v[76:77], v[30:31]
	v_mov_b64_e32 v[34:35], v[2:3]
	v_mov_b64_e32 v[38:39], v[6:7]
	v_mov_b64_e32 v[42:43], v[10:11]
	v_mov_b64_e32 v[46:47], v[14:15]
	v_mov_b64_e32 v[58:59], v[18:19]
	v_mov_b64_e32 v[62:63], v[22:23]
	v_mov_b64_e32 v[68:69], v[26:27]
	v_mov_b64_e32 v[72:73], v[30:31]
	v_mov_b64_e32 v[118:119], v[0:1]
	v_mov_b64_e32 v[110:111], v[4:5]
	v_mov_b64_e32 v[98:99], v[8:9]
	v_mov_b64_e32 v[94:95], v[12:13]
	v_mov_b64_e32 v[86:87], v[16:17]
	v_mov_b64_e32 v[82:83], v[20:21]
	v_mov_b64_e32 v[78:79], v[24:25]
	v_mov_b64_e32 v[74:75], v[28:29]
	s_waitcnt vmcnt(7)
	v_mov_b32_e32 v244, v138
	v_mov_b32_e32 v245, v139
	s_waitcnt vmcnt(6)
	v_mov_b32_e32 v242, v140
	v_mov_b32_e32 v243, v141
	s_waitcnt vmcnt(5)
	v_mov_b32_e32 v240, v142
	v_mov_b32_e32 v241, v143
	s_waitcnt vmcnt(4)
	v_mov_b32_e32 v238, v144
	v_mov_b32_e32 v239, v145
	s_waitcnt vmcnt(3)
	v_mov_b32_e32 v236, v148
	v_mov_b32_e32 v237, v149
	s_waitcnt vmcnt(2)
	v_mov_b32_e32 v234, v152
	v_mov_b32_e32 v235, v153
	s_waitcnt vmcnt(1)
	v_mov_b32_e32 v232, v154
	v_mov_b32_e32 v233, v155
	s_waitcnt vmcnt(0)
	v_mov_b32_e32 v230, v156
	v_mov_b32_e32 v231, v157
	v_mov_b64_e32 v[32:33], v[0:1]
	v_mov_b64_e32 v[36:37], v[4:5]
	v_mov_b64_e32 v[40:41], v[8:9]
	v_mov_b64_e32 v[44:45], v[12:13]
	v_mov_b64_e32 v[56:57], v[16:17]
	v_mov_b64_e32 v[60:61], v[20:21]
	v_mov_b64_e32 v[66:67], v[24:25]
	v_mov_b64_e32 v[70:71], v[28:29]
	s_branch .LBB0_1367
